# v51: window/SWA sub-tile1 K-frag LDS reads hoisted into sub-tile0 after QK MFMAs (issue block left in place)
# speedup vs baseline: 1.0178x; 1.0178x over previous
.Lw_win_4_done:
.LBB0_519:
	s_cmp_eq_u32 s32, 0
	s_cselect_b32 s84, 0, 1
	s_sub_u32 s32, s32, s84
	s_add_i32 s2, s29, s22
	s_add_i32 s3, s27, s21
	s_add_i32 s3, s3, -1
	s_and_b32 s31, s30, 0xc000
	s_add_i32 s33, s31, 0
	s_ashr_i32 s3, s3, 2
	s_add_i32 s31, s2, 0x7e0
	s_cmp_gt_i32 s31, s23
	v_cvt_f32_i32_e32 v111, s3
	s_cselect_b64 s[34:35], -1, 0
	s_add_i32 s3, s2, 0x7ff
	s_cmp_lt_i32 s3, s24
	s_cselect_b64 s[38:39], -1, 0
	v_add_u32_e32 v2, s33, v101
	v_add_u32_e32 v4, s33, v102
	v_add_u32_e32 v5, s33, v103
	v_add_u32_e32 v6, s33, v104
	s_or_b64 s[34:35], s[34:35], s[38:39]
	s_and_b64 vcc, exec, s[34:35]
	v_add_u32_e32 v115, v2, v100
	v_add_u32_e32 v114, v4, v100
	v_add_u32_e32 v113, v5, v100
	v_add_u32_e32 v112, v6, v100
	v_add_u32_e32 v16, s33, v105
	v_add_u32_e32 v17, s33, v106
	s_barrier
	s_cbranch_vccnz .Lkpre_skip_w
	ds_read_b128 v[4:7], v115 offset:4096
	ds_read_b128 v[188:191], v114 offset:4096
	ds_read_b128 v[192:195], v113 offset:4096
	ds_read_b128 v[202:205], v112 offset:4096
	s_and_b32 s31, s31, 0xe0
	v_or_b32_e32 v2, s31, v99
	v_cvt_f32_ubyte0_e32 v2, v2
	v_and_b32_e32 v2, 0x7fff0000, v2
	v_or_b32_sdwa v2, v2, v111 dst_sel:DWORD dst_unused:UNUSED_PAD src0_sel:DWORD src1_sel:WORD_1
	v_cndmask_b32_e64 v246, 0, v2, s[36:37]
	s_cmp_ge_i32 s20, s3
	s_cselect_b64 s[34:35], -1, 0
	s_waitcnt lgkmcnt(3)
	s_setprio 1
	v_mfma_f32_32x32x16_bf16 v[50:65], v[4:7], v[74:77], 0
	s_sub_i32 s3, s19, 32
	s_cmpk_lt_i32 s3, 0x1e1
	v_add3_u32 v116, v17, v94, s69
	s_cselect_b64 s[38:39], -1, 0
	s_and_b64 s[34:35], s[34:35], s[38:39]
	s_and_b64 vcc, exec, s[34:35]
	s_waitcnt lgkmcnt(2)
	v_mfma_f32_32x32x16_bf16 v[50:65], v[188:191], v[66:69], v[50:65]
	s_waitcnt lgkmcnt(1)
	v_mfma_f32_32x32x16_bf16 v[50:65], v[192:195], v[70:73], v[50:65]
	s_waitcnt lgkmcnt(0)
	v_mfma_f32_32x32x16_bf16 v[50:65], v[202:205], v[78:81], v[50:65]
	v_mfma_f32_32x32x16_bf16 v[50:65], v[246:249], v[82:85], v[50:65]
	v_add3_u32 v2, v16, v94, s69
	ds_read_b64_tr_b16 v[86:87], v2
	ds_read_b64_tr_b16 v[88:89], v2 offset:1024
	ds_read_b64_tr_b16 v[12:13], v116
	ds_read_b64_tr_b16 v[14:15], v116 offset:1024
	ds_read_b64_tr_b16 v[8:9], v2 offset:2048
	ds_read_b64_tr_b16 v[10:11], v2 offset:3072
	ds_read_b64_tr_b16 v[4:5], v116 offset:2048
	ds_read_b64_tr_b16 v[6:7], v116 offset:3072
	ds_read_b128 v[188:191], v115
	ds_read_b128 v[192:195], v114
	ds_read_b128 v[202:205], v113
	s_cbranch_vccnz .LBB0_524
	v_add_u32_e32 v2, s19, v108
	v_subrev_u32_e32 v116, 32, v2
	v_cmp_gt_u32_e32 vcc, s79, v116
	v_add3_u32 v116, v109, s22, 32
	s_nop 5
	v_cndmask_b32_e32 v50, v197, v50, vcc
	v_cmp_lt_u32_e32 vcc, s80, v116
	v_subrev_u32_e32 v116, 34, v2
	s_nop 0
	v_cndmask_b32_e32 v51, v197, v51, vcc
	v_cmp_gt_u32_e32 vcc, s79, v116
	v_subrev_u32_e32 v116, 35, v2
	s_nop 0
	v_cndmask_b32_e32 v52, v197, v52, vcc
	v_cmp_gt_u32_e32 vcc, s79, v116
	v_subrev_u32_e32 v116, 40, v2
	s_nop 0
	v_cndmask_b32_e32 v53, v197, v53, vcc
	v_cmp_gt_u32_e32 vcc, s79, v116
	v_subrev_u32_e32 v116, 41, v2
	s_nop 0
	v_cndmask_b32_e32 v54, v197, v54, vcc
	v_cmp_gt_u32_e32 vcc, s79, v116
	v_subrev_u32_e32 v116, 42, v2
	s_nop 0
	v_cndmask_b32_e32 v55, v197, v55, vcc
	v_cmp_gt_u32_e32 vcc, s79, v116
	v_subrev_u32_e32 v116, 43, v2
	s_nop 0
	v_cndmask_b32_e32 v56, v197, v56, vcc
	v_cmp_gt_u32_e32 vcc, s79, v116
	v_subrev_u32_e32 v116, 48, v2
	s_nop 0
	v_cndmask_b32_e32 v57, v197, v57, vcc
	v_cmp_gt_u32_e32 vcc, s79, v116
	v_subrev_u32_e32 v116, 49, v2
	s_nop 0
	v_cndmask_b32_e32 v58, v197, v58, vcc
	v_cmp_gt_u32_e32 vcc, s79, v116
	v_subrev_u32_e32 v116, 50, v2
	s_nop 0
	v_cndmask_b32_e32 v59, v197, v59, vcc
	v_cmp_gt_u32_e32 vcc, s79, v116
	v_subrev_u32_e32 v116, 51, v2
	s_nop 0
	v_cndmask_b32_e32 v60, v197, v60, vcc
	v_cmp_gt_u32_e32 vcc, s79, v116
	v_subrev_u32_e32 v116, 56, v2
	s_nop 0
	v_cndmask_b32_e32 v61, v197, v61, vcc
	v_cmp_gt_u32_e32 vcc, s79, v116
	v_subrev_u32_e32 v116, 57, v2
	s_nop 0
	v_cndmask_b32_e32 v62, v197, v62, vcc
	v_cmp_gt_u32_e32 vcc, s79, v116
	v_subrev_u32_e32 v116, 58, v2
	v_subrev_u32_e32 v2, 59, v2
	v_cndmask_b32_e32 v63, v197, v63, vcc
	v_cmp_gt_u32_e32 vcc, s79, v116
	s_nop 1
	v_cndmask_b32_e32 v64, v197, v64, vcc
	v_cmp_gt_u32_e32 vcc, s79, v2
	s_nop 1
	v_cndmask_b32_e32 v65, v197, v65, vcc

.Lw_swa_4_done:
.LBB0_780:
	s_cmp_eq_u32 s32, 0
	s_cselect_b32 s84, 0, 1
	s_sub_u32 s32, s32, s84
	s_add_i32 s0, s25, s17
	s_add_i32 s1, s23, s18
	s_add_i32 s1, s1, -1
	s_and_b32 s27, s26, 0xc000
	s_add_i32 s34, s27, 0
	s_ashr_i32 s1, s1, 2
	s_add_i32 s27, s0, 0x7e0
	s_cmp_gt_i32 s27, s19
	v_cvt_f32_i32_e32 v114, s1
	s_cselect_b64 s[28:29], -1, 0
	s_add_i32 s1, s0, 0x7ff
	s_cmp_lt_i32 s1, s20
	s_cselect_b64 s[30:31], -1, 0
	v_add_u32_e32 v2, s34, v104
	v_add_u32_e32 v4, s34, v105
	v_add_u32_e32 v5, s34, v106
	v_add_u32_e32 v6, s34, v107
	s_or_b64 s[28:29], s[28:29], s[30:31]
	s_and_b64 vcc, exec, s[28:29]
	v_add_u32_e32 v118, v2, v103
	v_add_u32_e32 v117, v4, v103
	v_add_u32_e32 v116, v5, v103
	v_add_u32_e32 v115, v6, v103
	v_add_u32_e32 v16, s34, v109
	v_add_u32_e32 v17, s34, v110
	s_barrier
	s_cbranch_vccnz .Lkpre_skip_s
	ds_read_b128 v[4:7], v118 offset:4096
	ds_read_b128 v[188:191], v117 offset:4096
	ds_read_b128 v[192:195], v116 offset:4096
	ds_read_b128 v[202:205], v115 offset:4096
	s_and_b32 s27, s27, 0xe0
	v_or_b32_e32 v2, s27, v102
	v_cvt_f32_ubyte0_e32 v2, v2
	v_and_b32_e32 v2, 0x7fff0000, v2
	v_or_b32_sdwa v2, v2, v114 dst_sel:DWORD dst_unused:UNUSED_PAD src0_sel:DWORD src1_sel:WORD_1
	v_cndmask_b32_e64 v246, 0, v2, s[36:37]
	s_cmp_ge_i32 s16, s1
	s_cselect_b64 s[28:29], -1, 0
	s_waitcnt lgkmcnt(3)
	s_setprio 1
	v_mfma_f32_32x32x16_bf16 v[50:65], v[4:7], v[66:69], 0
	s_sub_i32 s1, s15, 32
	s_cmpk_lt_i32 s1, 0x61
	v_add3_u32 v119, v17, v96, s69
	s_cselect_b64 s[30:31], -1, 0
	s_and_b64 s[28:29], s[28:29], s[30:31]
	s_and_b64 vcc, exec, s[28:29]
	s_waitcnt lgkmcnt(2)
	v_mfma_f32_32x32x16_bf16 v[50:65], v[188:191], v[70:73], v[50:65]
	s_waitcnt lgkmcnt(1)
	v_mfma_f32_32x32x16_bf16 v[50:65], v[192:195], v[74:77], v[50:65]
	s_waitcnt lgkmcnt(0)
	v_mfma_f32_32x32x16_bf16 v[50:65], v[202:205], v[78:81], v[50:65]
	v_mfma_f32_32x32x16_bf16 v[50:65], v[246:249], v[82:85], v[50:65]
	v_add3_u32 v2, v16, v96, s69
	ds_read_b64_tr_b16 v[86:87], v2
	ds_read_b64_tr_b16 v[88:89], v2 offset:1024
	ds_read_b64_tr_b16 v[12:13], v119
	ds_read_b64_tr_b16 v[14:15], v119 offset:1024
	ds_read_b64_tr_b16 v[8:9], v2 offset:2048
	ds_read_b64_tr_b16 v[10:11], v2 offset:3072
	ds_read_b64_tr_b16 v[4:5], v119 offset:2048
	ds_read_b64_tr_b16 v[6:7], v119 offset:3072
	ds_read_b128 v[188:191], v118
	ds_read_b128 v[192:195], v117
	ds_read_b128 v[202:205], v116
	s_cbranch_vccnz .LBB0_785
	v_add_u32_e32 v2, s15, v111
	v_subrev_u32_e32 v119, 32, v2
	v_cmp_gt_u32_e32 vcc, s71, v119
	v_add3_u32 v119, v112, s17, 32
	s_nop 5
	v_cndmask_b32_e32 v50, v197, v50, vcc
	v_cmp_lt_u32_e32 vcc, s47, v119
	v_subrev_u32_e32 v119, 34, v2
	s_nop 0
	v_cndmask_b32_e32 v51, v197, v51, vcc
	v_cmp_gt_u32_e32 vcc, s71, v119
	v_subrev_u32_e32 v119, 35, v2
	s_nop 0
	v_cndmask_b32_e32 v52, v197, v52, vcc
	v_cmp_gt_u32_e32 vcc, s71, v119
	v_subrev_u32_e32 v119, 40, v2
	s_nop 0
	v_cndmask_b32_e32 v53, v197, v53, vcc
	v_cmp_gt_u32_e32 vcc, s71, v119
	v_subrev_u32_e32 v119, 41, v2
	s_nop 0
	v_cndmask_b32_e32 v54, v197, v54, vcc
	v_cmp_gt_u32_e32 vcc, s71, v119
	v_subrev_u32_e32 v119, 42, v2
	s_nop 0
	v_cndmask_b32_e32 v55, v197, v55, vcc
	v_cmp_gt_u32_e32 vcc, s71, v119
	v_subrev_u32_e32 v119, 43, v2
	s_nop 0
	v_cndmask_b32_e32 v56, v197, v56, vcc
	v_cmp_gt_u32_e32 vcc, s71, v119
	v_subrev_u32_e32 v119, 48, v2
	s_nop 0
	v_cndmask_b32_e32 v57, v197, v57, vcc
	v_cmp_gt_u32_e32 vcc, s71, v119
	v_subrev_u32_e32 v119, 49, v2
	s_nop 0
	v_cndmask_b32_e32 v58, v197, v58, vcc
	v_cmp_gt_u32_e32 vcc, s71, v119
	v_subrev_u32_e32 v119, 50, v2
	s_nop 0
	v_cndmask_b32_e32 v59, v197, v59, vcc
	v_cmp_gt_u32_e32 vcc, s71, v119
	v_subrev_u32_e32 v119, 51, v2
	s_nop 0
	v_cndmask_b32_e32 v60, v197, v60, vcc
	v_cmp_gt_u32_e32 vcc, s71, v119
	v_subrev_u32_e32 v119, 56, v2
	s_nop 0
	v_cndmask_b32_e32 v61, v197, v61, vcc
	v_cmp_gt_u32_e32 vcc, s71, v119
	v_subrev_u32_e32 v119, 57, v2
	s_nop 0
	v_cndmask_b32_e32 v62, v197, v62, vcc
	v_cmp_gt_u32_e32 vcc, s71, v119
	v_subrev_u32_e32 v119, 58, v2
	v_subrev_u32_e32 v2, 59, v2
	v_cndmask_b32_e32 v63, v197, v63, vcc
	v_cmp_gt_u32_e32 vcc, s71, v119
	s_nop 1
	v_cndmask_b32_e32 v64, v197, v64, vcc
	v_cmp_gt_u32_e32 vcc, s71, v2
	s_nop 1
	v_cndmask_b32_e32 v65, v197, v65, vcc
